# v47 + waves 4-7: tile-type flag computation hoisted from between P.V and the score section to before P.V
# baseline (speedup 1.0000x reference)
.LBB0_187:
	v_add_u32_e32 v0, s44, v224
	s_add_i32 s44, s73, 0xfffffdb2
	s_cmp_gt_u32 s44, 0xfffffb44
	s_cselect_b64 s[42:43], -1, 0
	s_cmp_lt_u32 s44, 0xfffffb45
	s_cselect_b64 vcc, -1, 0
	s_cmp_gt_i32 s73, -1
	s_cselect_b64 s[44:45], -1, 0
	s_xor_b64 s[44:45], s[0:1], s[44:45]
	v_add_u32_e32 v212, s71, v243
	s_and_b64 s[44:45], vcc, s[44:45]
	v_add_u32_e32 v213, 0x21700, v212
	s_and_b64 vcc, exec, vcc
	s_cmp_eq_u32 s71, 0
	s_cbranch_scc1 .LBB0_189
.LBB0_188:
	s_waitcnt lgkmcnt(0)
	ds_read_b64_tr_b16 v[160:161], v0 offset:0
	ds_read_b64_tr_b16 v[162:163], v0 offset:0x800
	ds_read_b64_tr_b16 v[164:165], v0 offset:0x200
	ds_read_b64_tr_b16 v[166:167], v0 offset:0xa00
	ds_read_b64_tr_b16 v[168:169], v0 offset:0x400
	ds_read_b64_tr_b16 v[170:171], v0 offset:0xc00
	ds_read_b64_tr_b16 v[172:173], v0 offset:0x600
	ds_read_b64_tr_b16 v[174:175], v0 offset:0xe00
	s_waitcnt lgkmcnt(4)
	s_nop 0
	v_mfma_f32_32x32x16_bf16 v[112:127], v[208:211], v[160:163], v[112:127]
	v_mfma_f32_32x32x16_bf16 v[96:111], v[208:211], v[164:167], v[96:111]
	v_mfma_f32_32x32x16_bf16 v[128:143], v[156:159], v[160:163], v[128:143]
	v_mfma_f32_32x32x16_bf16 v[80:95], v[156:159], v[164:167], v[80:95]
	ds_read_b64_tr_b16 v[160:161], v0 offset:0x1000
	ds_read_b64_tr_b16 v[162:163], v0 offset:0x1800
	ds_read_b64_tr_b16 v[164:165], v0 offset:0x1200
	ds_read_b64_tr_b16 v[166:167], v0 offset:0x1a00
	s_waitcnt lgkmcnt(4)
	v_mfma_f32_32x32x16_bf16 v[64:79], v[208:211], v[168:171], v[64:79]
	v_mfma_f32_32x32x16_bf16 v[48:63], v[208:211], v[172:175], v[48:63]
	v_mfma_f32_32x32x16_bf16 v[32:47], v[156:159], v[168:171], v[32:47]
	v_mfma_f32_32x32x16_bf16 v[16:31], v[156:159], v[172:175], v[16:31]
	ds_read_b64_tr_b16 v[156:157], v0 offset:0x1400
	ds_read_b64_tr_b16 v[158:159], v0 offset:0x1c00
	ds_read_b64_tr_b16 v[168:169], v0 offset:0x1600
	ds_read_b64_tr_b16 v[170:171], v0 offset:0x1e00
	s_waitcnt lgkmcnt(4)
	v_mfma_f32_32x32x16_bf16 v[112:127], v[10:13], v[160:163], v[112:127]
	v_mfma_f32_32x32x16_bf16 v[96:111], v[10:13], v[164:167], v[96:111]
	v_mfma_f32_32x32x16_bf16 v[128:143], v[152:155], v[160:163], v[128:143]
	v_mfma_f32_32x32x16_bf16 v[80:95], v[152:155], v[164:167], v[80:95]
	ds_read_b64_tr_b16 v[160:161], v0 offset:0x2000
	ds_read_b64_tr_b16 v[162:163], v0 offset:0x2800
	ds_read_b64_tr_b16 v[164:165], v0 offset:0x2200
	ds_read_b64_tr_b16 v[166:167], v0 offset:0x2a00
	s_waitcnt lgkmcnt(4)
	v_mfma_f32_32x32x16_bf16 v[64:79], v[10:13], v[156:159], v[64:79]
	v_mfma_f32_32x32x16_bf16 v[48:63], v[10:13], v[168:171], v[48:63]
	v_mfma_f32_32x32x16_bf16 v[32:47], v[152:155], v[156:159], v[32:47]
	v_mfma_f32_32x32x16_bf16 v[16:31], v[152:155], v[168:171], v[16:31]
	ds_read_b64_tr_b16 v[10:11], v0 offset:0x2400
	ds_read_b64_tr_b16 v[12:13], v0 offset:0x2c00
	ds_read_b64_tr_b16 v[152:153], v0 offset:0x2600
	ds_read_b64_tr_b16 v[154:155], v0 offset:0x2e00
	s_waitcnt lgkmcnt(4)
	v_mfma_f32_32x32x16_bf16 v[112:127], v[6:9], v[160:163], v[112:127]
	v_mfma_f32_32x32x16_bf16 v[96:111], v[6:9], v[164:167], v[96:111]
	v_mfma_f32_32x32x16_bf16 v[128:143], v[148:151], v[160:163], v[128:143]
	v_mfma_f32_32x32x16_bf16 v[80:95], v[148:151], v[164:167], v[80:95]
	ds_read_b64_tr_b16 v[156:157], v0 offset:0x3000
	ds_read_b64_tr_b16 v[158:159], v0 offset:0x3800
	ds_read_b64_tr_b16 v[160:161], v0 offset:0x3200
	ds_read_b64_tr_b16 v[162:163], v0 offset:0x3a00
	s_waitcnt lgkmcnt(4)
	v_mfma_f32_32x32x16_bf16 v[64:79], v[6:9], v[10:13], v[64:79]
	v_mfma_f32_32x32x16_bf16 v[48:63], v[6:9], v[152:155], v[48:63]
	v_mfma_f32_32x32x16_bf16 v[32:47], v[148:151], v[10:13], v[32:47]
	v_mfma_f32_32x32x16_bf16 v[16:31], v[148:151], v[152:155], v[16:31]
	ds_read_b64_tr_b16 v[6:7], v0 offset:0x3400
	ds_read_b64_tr_b16 v[8:9], v0 offset:0x3c00
	ds_read_b64_tr_b16 v[10:11], v0 offset:0x3600
	ds_read_b64_tr_b16 v[12:13], v0 offset:0x3e00
	s_waitcnt lgkmcnt(4)
	v_mfma_f32_32x32x16_bf16 v[112:127], v[2:5], v[156:159], v[112:127]
	v_mfma_f32_32x32x16_bf16 v[96:111], v[2:5], v[160:163], v[96:111]
	v_mfma_f32_32x32x16_bf16 v[128:143], v[144:147], v[156:159], v[128:143]
	v_mfma_f32_32x32x16_bf16 v[80:95], v[144:147], v[160:163], v[80:95]
	s_waitcnt lgkmcnt(0)
	v_mfma_f32_32x32x16_bf16 v[64:79], v[2:5], v[6:9], v[64:79]
	v_mfma_f32_32x32x16_bf16 v[48:63], v[2:5], v[10:13], v[48:63]
	v_mfma_f32_32x32x16_bf16 v[32:47], v[144:147], v[6:9], v[32:47]
	v_mfma_f32_32x32x16_bf16 v[16:31], v[144:147], v[10:13], v[16:31]
.LBB0_189:
	s_cbranch_vccnz .LBB0_194
	v_add_u32_e32 v0, 0x21780, v212
	v_add_u32_e32 v2, 0x21708, v212
	v_add_u32_e32 v3, 0x21788, v212
	ds_read2_b32 v[144:145], v213 offset1:1
	ds_read2_b32 v[160:161], v0 offset1:1
	ds_read2_b32 v[146:147], v2 offset1:1
	ds_read2_b32 v[162:163], v3 offset1:1
	v_add_u32_e32 v0, 0x21720, v212
	v_add_u32_e32 v2, 0x217a0, v212
	v_add_u32_e32 v3, 0x21728, v212
	v_add_u32_e32 v4, 0x217a8, v212
	ds_read2_b32 v[148:149], v0 offset1:1
	ds_read2_b32 v[164:165], v2 offset1:1
	ds_read2_b32 v[150:151], v3 offset1:1
	ds_read2_b32 v[166:167], v4 offset1:1
	v_add_u32_e32 v0, 0x21740, v212
	v_add_u32_e32 v2, 0x217c0, v212
	v_add_u32_e32 v3, 0x21748, v212
	v_add_u32_e32 v4, 0x217c8, v212
	ds_read2_b32 v[152:153], v0 offset1:1
	ds_read2_b32 v[168:169], v2 offset1:1
	ds_read2_b32 v[154:155], v3 offset1:1
	ds_read2_b32 v[170:171], v4 offset1:1
	v_add_u32_e32 v0, 0x21760, v212
	v_add_u32_e32 v2, 0x217e0, v212
	v_add_u32_e32 v3, 0x21768, v212
	v_add_u32_e32 v4, 0x217e8, v212
	ds_read2_b32 v[156:157], v0 offset1:1
	ds_read2_b32 v[172:173], v2 offset1:1
	ds_read2_b32 v[158:159], v3 offset1:1
	ds_read2_b32 v[174:175], v4 offset1:1
	s_branch .LBB0_195

.LBB0_193:
	s_add_i32 s42, s7, s90
	v_lshl_add_u64 v[14:15], s[40:41], 0, v[218:219]
	s_mov_b32 m0, s42
	s_nop 0
	global_load_lds_dwordx4 v[14:15], off
	v_lshl_add_u64 v[14:15], s[40:41], 0, v[214:215]
	s_add_i32 m0, s42, 0x400
	s_add_i32 s42, s3, s90
	global_load_lds_dwordx4 v[14:15], off
	v_lshl_add_u64 v[14:15], s[40:41], 0, v[216:217]
	v_lshl_add_u64 v[160:161], v[14:15], 0, s[24:25]
	s_mov_b32 m0, s42
	v_lshl_add_u64 v[14:15], v[14:15], 0, s[26:27]
	global_load_lds_dwordx4 v[160:161], off
	s_add_i32 m0, s42, 0x400
	s_nop 0
	global_load_lds_dwordx4 v[14:15], off
	s_branch .LBB0_187
